# P5: head 0's z pieces loaded straight into place in the unit set-up (no wait before the head loop)
# baseline (speedup 1.0000x reference)
.LBB0_563:
	s_lshr_b32 s0, s49, 3
	s_and_b32 s6, s0, 63
	v_readlane_b32 s0, v255, 55
	s_and_b32 s0, s0, 7
	v_readlane_b32 s56, v253, 18
	v_lshl_or_b32 v2, s0, 9, v165
	v_readlane_b32 s8, v255, 53
	v_lshlrev_b32_e32 v160, 1, v2
	v_lshlrev_b32_e32 v12, 2, v2
	v_mov_b32_e32 v13, v161
	v_readlane_b32 s66, v253, 28
	v_readlane_b32 s67, v253, 29
	v_readlane_b32 s9, v255, 54
	v_cndmask_b32_e64 v2, v1, 0, s[80:81]
	v_lshl_add_u64 v[110:111], s[66:67], 0, v[12:13]
	v_lshl_add_u64 v[112:113], s[8:9], 0, v[12:13]
	v_cndmask_b32_e64 v1, v205, 0, s[80:81]
	v_cndmask_b32_e64 v12, v206, 0, s[80:81]
	v_lshlrev_b32_e32 v13, 16, v2
	v_fma_f32 v13, v176, v13, v184
	v_and_b32_e32 v70, 0xffff0000, v2
	v_lshlrev_b32_e32 v81, 16, v1
	v_lshlrev_b32_e32 v85, 16, v12
	v_lshlrev_b32_e32 v84, 16, v3
	v_mov_b32_e32 v74, v182
	v_mov_b32_e32 v75, v180
	v_fma_f32 v80, v177, v70, v185
	v_fmac_f32_e32 v13, v178, v81
	v_pk_mul_f32 v[70:71], v[74:75], v[84:85]
	v_and_b32_e32 v83, 0xffff0000, v1
	v_add_f32_e32 v13, v71, v13
	v_add_f32_e32 v13, v70, v13
	v_mul_f32_e32 v70, 0xbfb8aa3b, v13
	v_exp_f32_e32 v82, v70
	v_and_b32_e32 v91, 0xffff0000, v12
	v_and_b32_e32 v90, 0xffff0000, v3
	v_mov_b32_e32 v92, v183
	v_add_f32_e32 v82, 1.0, v82
	v_rcp_f32_e32 v82, v82
	v_mov_b32_e32 v93, v181
	v_fmac_f32_e32 v80, v179, v83
	v_pk_mul_f32 v[94:95], v[92:93], v[90:91]
	v_mul_f32_e32 v13, v13, v82
	v_add_f32_e32 v80, v95, v80
	v_add_f32_e32 v82, v94, v80
	v_mul_f32_e32 v80, 0xbfb8aa3b, v82
	v_exp_f32_e32 v80, v80
	ds_read_b128 v[76:79], v242
	ds_read_b128 v[70:73], v242 offset:16
	v_mov_b32_e32 v94, v178
	v_mov_b32_e32 v95, v176
	v_add_f32_e32 v80, 1.0, v80
	v_rcp_f32_e32 v98, v80
	v_mov_b32_e32 v80, v85
	v_lshlrev_b32_e32 v87, 16, v4
	v_lshlrev_b32_e32 v86, 16, v5
	v_pk_mul_f32 v[80:81], v[94:95], v[80:81]
	v_mul_f32_e32 v82, v82, v98
	s_waitcnt lgkmcnt(1)
	v_mul_f32_e32 v13, v13, v76
	v_pk_mul_f32 v[96:97], v[94:95], v[84:85]
	v_mul_f32_e32 v106, v82, v76
	v_pk_mov_b32 v[84:85], v[86:87], v[84:85] op_sel:[1,0]
	v_add_f32_e32 v76, v81, v184
	v_pk_mul_f32 v[104:105], v[74:75], v[84:85]
	v_add_f32_e32 v76, v80, v76
	v_add_f32_e32 v76, v105, v76
	v_add_f32_e32 v76, v104, v76
	v_mul_f32_e32 v80, 0xbfb8aa3b, v76
	v_add_f32_e32 v97, v97, v184
	v_exp_f32_e32 v104, v80
	v_pk_mul_f32 v[80:81], v[74:75], v[86:87]
	v_add_f32_e32 v96, v96, v97
	v_add_f32_e32 v81, v81, v96
	v_add_f32_e32 v96, v80, v81
	v_mul_f32_e32 v80, 0xbfb8aa3b, v96
	v_exp_f32_e32 v80, v80
	v_add_f32_e32 v97, 1.0, v104
	v_rcp_f32_e32 v97, v97
	v_mov_b32_e32 v98, v179
	v_add_f32_e32 v80, 1.0, v80
	v_rcp_f32_e32 v104, v80
	v_mov_b32_e32 v99, v177
	v_mov_b32_e32 v82, v91
	v_mul_f32_e32 v76, v76, v97
	v_and_b32_e32 v89, 0xffff0000, v4
	v_and_b32_e32 v88, 0xffff0000, v5
	v_pk_mul_f32 v[82:83], v[98:99], v[82:83]
	v_mul_f32_e32 v105, v76, v77
	v_mul_f32_e32 v76, v96, v104
	v_pk_mul_f32 v[100:101], v[98:99], v[90:91]
	v_mul_f32_e32 v104, v76, v78
	v_pk_mov_b32 v[90:91], v[88:89], v[90:91] op_sel:[1,0]
	v_add_f32_e32 v76, v83, v185
	v_pk_mul_f32 v[96:97], v[92:93], v[90:91]
	v_add_f32_e32 v76, v82, v76
	v_add_f32_e32 v76, v97, v76
	v_add_f32_e32 v76, v96, v76
	v_mul_f32_e32 v82, 0xbfb8aa3b, v76
	v_add_f32_e32 v97, v101, v185
	v_exp_f32_e32 v96, v82
	v_pk_mul_f32 v[82:83], v[92:93], v[88:89]
	v_add_f32_e32 v97, v100, v97
	v_add_f32_e32 v83, v83, v97
	v_add_f32_e32 v97, v82, v83
	v_mul_f32_e32 v82, 0xbfb8aa3b, v97
	v_exp_f32_e32 v100, v82
	v_pk_mul_f32 v[82:83], v[94:95], v[84:85]
	v_add_f32_e32 v84, 1.0, v96
	v_rcp_f32_e32 v96, v84
	v_add_f32_e32 v84, 1.0, v100
	v_rcp_f32_e32 v100, v84
	v_lshlrev_b32_e32 v103, 16, v6
	v_mul_f32_e32 v76, v76, v96
	v_lshlrev_b32_e32 v102, 16, v7
	v_mul_f32_e32 v107, v76, v77
	v_mul_f32_e32 v76, v97, v100
	v_pk_mul_f32 v[84:85], v[94:95], v[86:87]
	v_mul_f32_e32 v108, v76, v78
	v_pk_mov_b32 v[86:87], v[102:103], v[86:87] op_sel:[1,0]
	v_add_f32_e32 v78, v83, v184
	v_pk_mul_f32 v[100:101], v[74:75], v[86:87]
	v_add_f32_e32 v78, v82, v78
	v_add_f32_e32 v78, v101, v78
	v_add_f32_e32 v78, v100, v78
	v_mul_f32_e32 v82, 0xbfb8aa3b, v78
	v_add_f32_e32 v85, v85, v184
	v_exp_f32_e32 v100, v82
	v_pk_mul_f32 v[82:83], v[74:75], v[102:103]
	v_add_f32_e32 v84, v84, v85
	v_add_f32_e32 v83, v83, v84
	v_add_f32_e32 v84, v82, v83
	v_mul_f32_e32 v82, 0xbfb8aa3b, v84
	v_exp_f32_e32 v82, v82
	v_add_f32_e32 v85, 1.0, v100
	v_rcp_f32_e32 v85, v85
	v_and_b32_e32 v81, 0xffff0000, v6
	v_add_f32_e32 v82, 1.0, v82
	v_rcp_f32_e32 v100, v82
	v_and_b32_e32 v80, 0xffff0000, v7
	v_pk_mul_f32 v[76:77], v[98:99], v[90:91]
	v_mul_f32_e32 v78, v78, v85
	v_mul_f32_e32 v101, v78, v79
	v_mul_f32_e32 v78, v84, v100
	v_pk_mul_f32 v[84:85], v[94:95], v[86:87]
	v_pk_mov_b32 v[86:87], v[80:81], v[88:89] op_sel:[1,0]
	v_add_f32_e32 v77, v77, v185
	v_pk_mul_f32 v[90:91], v[98:99], v[88:89]
	v_pk_mul_f32 v[88:89], v[92:93], v[86:87]
	v_add_f32_e32 v76, v76, v77
	v_add_f32_e32 v76, v89, v76
	s_waitcnt lgkmcnt(0)
	v_mul_f32_e32 v100, v78, v70
	v_add_f32_e32 v78, v88, v76
	v_mul_f32_e32 v76, 0xbfb8aa3b, v78
	v_add_f32_e32 v89, v91, v185
	v_exp_f32_e32 v88, v76
	v_pk_mul_f32 v[76:77], v[92:93], v[80:81]
	v_add_f32_e32 v89, v90, v89
	v_add_f32_e32 v77, v77, v89
	v_add_f32_e32 v109, v76, v77
	v_mul_f32_e32 v76, 0xbfb8aa3b, v109
	v_exp_f32_e32 v89, v76
	v_add_f32_e32 v88, 1.0, v88
	v_lshlrev_b32_e32 v97, 16, v8
	v_lshlrev_b32_e32 v96, 16, v9
	v_rcp_f32_e32 v114, v88
	v_add_f32_e32 v88, 1.0, v89
	v_rcp_f32_e32 v115, v88
	v_pk_mov_b32 v[88:89], v[96:97], v[102:103] op_sel:[1,0]
	v_add_f32_e32 v85, v85, v184
	v_pk_mul_f32 v[90:91], v[74:75], v[88:89]
	v_add_f32_e32 v84, v84, v85
	v_add_f32_e32 v84, v91, v84
	v_add_f32_e32 v90, v90, v84
	v_mul_f32_e32 v84, 0xbfb8aa3b, v90
	v_exp_f32_e32 v84, v84
	v_mul_f32_e32 v78, v78, v114
	v_mul_f32_e32 v91, v78, v79
	v_mul_f32_e32 v78, v109, v115
	v_add_f32_e32 v79, 1.0, v84
	v_and_b32_e32 v83, 0xffff0000, v8
	v_and_b32_e32 v82, 0xffff0000, v9
	v_pk_mul_f32 v[76:77], v[94:95], v[102:103]
	v_rcp_f32_e32 v102, v79
	v_mul_f32_e32 v103, v78, v70
	v_pk_mul_f32 v[78:79], v[98:99], v[86:87]
	v_pk_mul_f32 v[84:85], v[98:99], v[80:81]
	v_pk_mov_b32 v[80:81], v[82:83], v[80:81] op_sel:[1,0]
	v_add_f32_e32 v79, v79, v185
	v_pk_mul_f32 v[86:87], v[92:93], v[80:81]
	v_add_f32_e32 v78, v78, v79
	v_add_f32_e32 v78, v87, v78
	v_add_f32_e32 v86, v86, v78
	v_mul_f32_e32 v78, 0xbfb8aa3b, v86
	v_exp_f32_e32 v87, v78
	v_mul_f32_e32 v70, v90, v102
	v_mul_f32_e32 v90, v70, v71
	v_add_f32_e32 v70, v77, v184
	v_add_f32_e32 v77, 1.0, v87
	v_rcp_f32_e32 v77, v77
	v_pk_mul_f32 v[78:79], v[74:75], v[96:97]
	v_add_f32_e32 v70, v76, v70
	v_add_f32_e32 v70, v79, v70
	v_add_f32_e32 v70, v78, v70
	v_mul_f32_e32 v78, v86, v77
	v_pk_mul_f32 v[76:77], v[92:93], v[82:83]
	v_mul_f32_e32 v83, 0xbfb8aa3b, v70
	v_exp_f32_e32 v83, v83
	v_add_f32_e32 v79, v85, v185
	v_add_f32_e32 v79, v84, v79
	v_add_f32_e32 v77, v77, v79
	v_add_f32_e32 v84, v76, v77
	v_add_f32_e32 v76, 1.0, v83
	v_rcp_f32_e32 v76, v76
	v_mul_f32_e32 v77, 0xbfb8aa3b, v84
	v_exp_f32_e32 v77, v77
	v_mul_f32_e32 v83, v78, v71
	v_mul_f32_e32 v70, v70, v76
	v_mul_f32_e32 v85, v70, v72
	v_add_f32_e32 v70, 1.0, v77
	v_rcp_f32_e32 v86, v70
	v_pk_mul_f32 v[70:71], v[94:95], v[88:89]
	v_lshlrev_b32_e32 v78, 16, v10
	v_mov_b32_e32 v79, v96
	v_add_f32_e32 v71, v71, v184
	v_pk_mul_f32 v[74:75], v[74:75], v[78:79]
	v_add_f32_e32 v70, v70, v71
	v_pk_mul_f32 v[76:77], v[98:99], v[80:81]
	v_add_f32_e32 v70, v75, v70
	v_add_f32_e32 v74, v74, v70
	v_and_b32_e32 v70, 0xffff0000, v10
	v_mov_b32_e32 v71, v82
	v_add_f32_e32 v75, v77, v185
	v_pk_mul_f32 v[70:71], v[92:93], v[70:71]
	v_add_f32_e32 v75, v76, v75
	v_add_f32_e32 v71, v71, v75
	v_add_f32_e32 v70, v70, v71
	v_mul_f32_e32 v75, 0xbfb8aa3b, v70
	v_mul_f32_e32 v71, 0xbfb8aa3b, v74
	v_exp_f32_e32 v75, v75
	v_exp_f32_e32 v71, v71
	s_lshl_b32 s1, s6, 7
	s_add_i32 s6, s5, s6
	v_add_f32_e32 v75, 1.0, v75
	v_add_f32_e32 v71, 1.0, v71
	v_rcp_f32_e32 v75, v75
	v_rcp_f32_e32 v71, v71
	s_ashr_i32 s7, s6, 31
	s_lshl_b64 s[6:7], s[6:7], 20
	v_mul_f32_e32 v70, v70, v75
	v_mul_f32_e32 v76, v84, v86
	v_mul_f32_e32 v71, v74, v71
	v_mul_f32_e32 v78, v70, v73
	v_cvt_pk_bf16_f32 v70, v13, v105
	v_or_b32_e32 v13, s6, v170
	s_add_i32 s1, s1, s4
	v_mul_f32_e32 v77, v76, v72
	v_mul_f32_e32 v74, v71, v73
	v_cvt_pk_bf16_f32 v71, v104, v101
	v_cvt_pk_bf16_f32 v72, v100, v90
	v_cvt_pk_bf16_f32 v73, v85, v74
	v_lshl_or_b32 v114, s0, 17, v13
	v_add_u32_e32 v13, s1, v211
	v_cvt_pk_bf16_f32 v74, v106, v107
	v_cvt_pk_bf16_f32 v75, v108, v91
	v_cvt_pk_bf16_f32 v76, v103, v83
	v_cvt_pk_bf16_f32 v77, v77, v78
	ds_write_b128 v227, v[70:73]
	ds_write_b128 v227, v[74:77] offset:272
	ds_write_b128 v229, v[14:17]
	ds_write_b128 v231, v[18:21]
	v_mad_i64_i32 v[70:71], s[4:5], v13, s11, v[160:161]
	v_add_u32_e32 v13, s1, v171
	v_mov_b32_e32 v115, s7
	s_mov_b64 s[6:7], 0x45c00080
	v_mad_i64_i32 v[118:119], s[4:5], v13, s11, v[160:161]
	v_add_u32_e32 v13, s1, v204
	v_lshl_add_u64 v[116:117], v[70:71], 0, s[6:7]
	v_mad_i64_i32 v[70:71], s[4:5], v13, s11, v[160:161]
	v_add_u32_e32 v13, s1, v163
	v_lshl_add_u64 v[120:121], v[70:71], 0, s[6:7]
	v_mad_i64_i32 v[70:71], s[4:5], v13, s11, v[160:161]
	v_add_u32_e32 v13, s1, v173
	v_lshl_add_u64 v[122:123], v[70:71], 0, s[6:7]
	v_mad_i64_i32 v[70:71], s[4:5], v13, s11, v[160:161]
	v_lshl_add_u64 v[124:125], v[70:71], 0, s[6:7]
	v_add_u32_e32 v70, s1, v232
	v_ashrrev_i32_e32 v71, 31, v70
	v_lshlrev_b64 v[126:127], 13, v[70:71]
	v_or_b32_e32 v13, v162, v126
	s_mov_b32 s2, 0
	v_lshl_or_b32 v126, s0, 10, v13
	v_lshl_add_u64 v[198:199], s[92:93], 0, v[126:127]
	v_add_co_u32_e32 v198, vcc, 0x3dc00000, v198
	s_nop 1
	v_addc_co_u32_e32 v199, vcc, 0, v199, vcc
	global_load_dwordx4 v[74:77], v[198:199], off
	global_load_dwordx4 v[70:73], v[198:199], off offset:64
	v_mov_b32_e32 v140, 0
	s_mov_b64 s[0:1], 0
	v_mov_b32_e32 v13, v245
	v_mov_b32_e32 v141, v244
	v_mov_b32_e32 v142, v243
	v_readlane_b32 s57, v253, 19
	v_readlane_b32 s58, v253, 20
	v_readlane_b32 s59, v253, 21
	v_readlane_b32 s60, v253, 22
	v_readlane_b32 s61, v253, 23
	v_readlane_b32 s62, v253, 24
	v_readlane_b32 s63, v253, 25
	v_readlane_b32 s64, v253, 26
	v_readlane_b32 s65, v253, 27
	v_readlane_b32 s68, v253, 30
	v_readlane_b32 s69, v253, 31
	v_readlane_b32 s70, v253, 32
	v_readlane_b32 s71, v253, 33
	s_waitcnt lgkmcnt(0)
	s_barrier
	s_branch .LBB0_565

.LBB0_565:
	v_lshl_add_u64 v[128:129], s[92:93], 0, v[126:127]
	s_mov_b32 s4, 0x3dc00000
	v_add_co_u32_e32 v198, vcc, s4, v128
	v_readlane_b32 s6, v11, s2
	s_nop 0
	v_addc_co_u32_e32 v199, vcc, 0, v129, vcc
	s_cmp_eq_u32 s2, 0
	s_cbranch_scc1 .Lp5_z0skip
	v_mov_b64_e32 v[74:75], v[200:201]
	v_mov_b64_e32 v[76:77], v[202:203]
	v_mov_b64_e32 v[70:71], v[216:217]
	v_mov_b64_e32 v[72:73], v[218:219]
.Lp5_z0skip:
	global_load_dwordx4 v[200:203], v[198:199], off offset:128
	global_load_dwordx4 v[216:219], v[198:199], off offset:192
	s_cmpk_eq_i32 s0, 0x700
	s_cbranch_scc1 .Lp5_pf_skip
	global_load_dword v2, v124, s[92:93]
	global_load_dword v1, v122, s[92:93]
	global_load_dword v12, v120, s[92:93]
	s_add_u32 s4, s92, 0x45c00000
	s_addc_u32 s5, s93, 0
	global_load_dword v3, v118, s[4:5] offset:128
	s_add_u32 s4, s4, 0x3000
	s_addc_u32 s5, s5, 0
	global_load_dword v4, v118, s[4:5] offset:128
	s_add_u32 s4, s4, 0x3000
	s_addc_u32 s5, s5, 0
	global_load_dword v5, v118, s[4:5] offset:128
	s_add_u32 s4, s4, 0x3000
	s_addc_u32 s5, s5, 0
	global_load_dword v6, v118, s[4:5] offset:128
	s_add_u32 s4, s4, 0x3000
	s_addc_u32 s5, s5, 0
	global_load_dword v7, v118, s[4:5] offset:128
	s_add_u32 s4, s4, 0x3000
	s_addc_u32 s5, s5, 0
	global_load_dword v8, v118, s[4:5] offset:128
	s_add_u32 s4, s4, 0x3000
	s_addc_u32 s5, s5, 0
	global_load_dword v9, v118, s[4:5] offset:128
	global_load_dword v10, v116, s[92:93]
	v_lshl_add_u64 v[14:15], v[110:111], 0, s[0:1]
	s_movk_i32 s4, 0x6000
	s_mov_b32 s5, 0
	global_load_dwordx2 v[176:177], v[14:15], off offset:256
	v_lshl_add_u64 v[14:15], v[14:15], 0, s[4:5]
	global_load_dwordx2 v[178:179], v[14:15], off offset:256
	v_lshl_add_u64 v[14:15], v[14:15], 0, s[4:5]
	global_load_dwordx2 v[180:181], v[14:15], off offset:256
	v_lshl_add_u64 v[14:15], v[14:15], 0, s[4:5]
	global_load_dwordx2 v[182:183], v[14:15], off offset:256
	v_lshl_add_u64 v[14:15], v[112:113], 0, s[0:1]
	global_load_dwordx2 v[184:185], v[14:15], off
	v_lshl_add_u64 v[94:95], s[92:93], 0, v[114:115]
	s_mov_b32 s4, 0x5e004000
	v_lshl_add_u64 v[16:17], v[94:95], 0, s[4:5]
	global_load_dwordx4 v[14:17], v[16:17], off
	s_mov_b32 s4, 0x5e006000
	v_lshl_add_u64 v[18:19], v[94:95], 0, s[4:5]
	global_load_dwordx4 v[18:21], v[18:19], off
